# attention phase: static s_setprio 1 for waves 4-7 (second-dispatched half), reset after the phase; on top of static wave-half priority in the GEMM phases
# baseline (speedup 1.0000x reference)
.LBB0_581:
	s_ashr_i32 s23, s22, 31
	s_lshl_b64 s[4:5], s[22:23], 2
	s_ashr_i32 s24, s31, 31
	s_add_u32 s1, s4, s31
	s_addc_u32 s4, s5, s24
	s_mulk_i32 s4, 0xc0
	s_mul_hi_u32 s5, s1, 0xc0
	s_add_i32 s5, s5, s4
	s_mulk_i32 s1, 0xc0
	s_add_u32 s4, s8, s1
	s_addc_u32 s5, s9, s5
	s_ashr_i32 s1, s0, 31
	s_lshl_b64 s[6:7], s[0:1], 2
	s_add_u32 s1, s6, s31
	s_addc_u32 s24, s7, s24
	s_mul_i32 s6, s24, 0x110000
	s_mul_hi_u32 s7, s1, 0x110000
	v_mov_b32_e32 v119, v0
	s_barrier
	v_readfirstlane_b32 s100, v0
	s_cmpk_gt_u32 s100, 0xff
	s_cbranch_scc0 .Lat_np
	s_setprio 1
.Lat_np:
	s_add_i32 s7, s7, s6
	s_mul_i32 s6, s1, 0x110000
	s_add_u32 s6, s10, s6
	v_ashrrev_i32_e32 v14, 4, v119
	s_mul_i32 s24, s24, 0x88000
	s_mul_hi_u32 s25, s1, 0x88000
	v_ashrrev_i32_e32 v15, 31, v14
	s_addc_u32 s7, s11, s7
	s_add_i32 s25, s25, s24
	s_mul_i32 s1, s1, 0x88000
	v_ashrrev_i32_e32 v16, 3, v119
	v_lshlrev_b32_e32 v58, 4, v119
	v_lshlrev_b64 v[52:53], 8, v[14:15]
	v_add_u32_e32 v20, 32, v14
	s_add_u32 s24, s12, s1
	v_lshlrev_b32_e32 v24, 3, v119
	v_ashrrev_i32_e32 v17, 31, v16
	v_lshl_add_u64 v[6:7], s[6:7], 0, v[52:53]
	v_and_b32_e32 v18, 0xf0, v58
	v_mov_b32_e32 v19, v227
	v_ashrrev_i32_e32 v21, 31, v20
	s_addc_u32 s25, s13, s25
	v_and_b32_e32 v4, 56, v24
	v_lshlrev_b64 v[50:51], 7, v[16:17]
	v_lshl_add_u64 v[56:57], v[6:7], 0, v[18:19]
	v_lshlrev_b64 v[6:7], 8, v[20:21]
	v_lshl_add_u64 v[2:3], s[24:25], 0, v[50:51]
	v_lshlrev_b32_e32 v4, 1, v4
	v_mov_b32_e32 v5, v227
	v_lshl_add_u64 v[6:7], s[6:7], 0, v[6:7]
	v_lshl_add_u64 v[54:55], v[2:3], 0, v[4:5]
	v_lshl_add_u64 v[10:11], v[6:7], 0, v[18:19]
	global_load_dwordx4 v[2:5], v[54:55], off
	global_load_dwordx4 v[6:9], v[56:57], off
	s_nop 0
	global_load_dwordx4 v[10:13], v[10:11], off
	v_ashrrev_i32_e32 v15, 1, v119
	s_movk_i32 s1, 0xffe0
	v_bfe_u32 v136, v119, 5, 1
	v_bfi_b32 v17, s1, v15, v119
	v_mov_b64_e32 v[22:23], s[4:5]
	s_movk_i32 s1, 0x300
	v_mad_i64_i32 v[22:23], s[4:5], v17, s1, v[22:23]
	v_lshlrev_b32_e32 v226, 4, v136
	v_lshl_add_u64 v[22:23], v[22:23], 0, v[226:227]
	global_load_dwordx4 v[86:89], v[22:23], off
	global_load_dwordx4 v[74:77], v[22:23], off offset:32
	global_load_dwordx4 v[70:73], v[22:23], off offset:64
	global_load_dwordx4 v[82:85], v[22:23], off offset:96
	global_load_dwordx4 v[78:81], v[22:23], off offset:128
	global_load_dwordx4 v[66:69], v[22:23], off offset:160
	v_and_b32_e32 v19, 0x1fffff0, v16
	v_lshlrev_b32_e32 v21, 1, v16
	v_and_b32_e32 v17, 0x70, v119
	v_lshrrev_b32_e32 v25, 1, v16
	v_and_b32_e32 v16, 3, v16
	v_lshlrev_b32_e32 v14, 8, v14
	v_and_or_b32 v19, v21, 8, v19
	v_bfe_u32 v24, v24, 5, 1
	v_and_b32_e32 v26, 48, v58
	v_and_or_b32 v16, v25, 4, v16
	v_bitop3_b32 v14, v18, v14, v17 bitop3:0xde
	v_lshlrev_b32_e32 v20, 8, v20
	v_lshrrev_b32_e32 v19, 2, v19
	v_lshl_or_b32 v16, v16, 6, v26
	v_add_u32_e32 v142, 0, v14
	v_bitop3_b32 v14, v18, v20, v17 bitop3:0xde
	v_or_b32_e32 v17, v19, v24
	v_add_u32_e32 v143, 0, v14
	v_lshl_or_b32 v14, v17, 9, v16
	v_and_b32_e32 v137, 31, v119
	v_add_u32_e32 v144, 0, v14
	v_lshlrev_b32_e32 v90, 8, v137
	s_waitcnt vmcnt(0)
	v_and_b32_e32 v132, 63, v119
	s_movk_i32 s1, 0x2000
	s_movk_i32 s6, 0x4000
	s_mov_b32 s4, 0xa000
	s_cmp_lg_u32 0, -1
	s_mul_i32 s24, s31, 0x110000
	s_waitcnt vmcnt(8)
	ds_write_b128 v144, v[2:5]
	s_waitcnt vmcnt(7)
	ds_write_b128 v142, v[6:9] offset:16384
	s_waitcnt vmcnt(6)
	ds_write_b128 v143, v[10:13] offset:16384
	v_and_b32_e32 v10, 0x70, v58
	v_bitop3_b32 v2, v226, v90, v10 bitop3:0xde
	v_add_u32_e32 v145, 0, v2
	s_waitcnt lgkmcnt(0)
	s_barrier
	ds_read_b128 v[2:5], v145 offset:16384
	ds_read_b128 v[6:9], v145 offset:24576
	s_waitcnt vmcnt(5) lgkmcnt(1)
	v_mfma_f32_32x32x16_bf16 v[18:33], v[2:5], v[86:89], 0
	v_or_b32_e32 v2, 32, v226
	v_bitop3_b32 v2, v2, v90, v10 bitop3:0xde
	v_add_u32_e32 v148, 0, v2
	v_lshlrev_b32_e32 v11, 3, v132
	v_lshlrev_b32_e32 v13, 1, v119
	s_mul_hi_i32 s7, s31, 0x110000
	s_mov_b32 s57, s56
	s_waitcnt lgkmcnt(0)
	v_mfma_f32_32x32x16_bf16 v[34:49], v[6:9], v[86:89], 0
	ds_read_b128 v[2:5], v148 offset:16384
	ds_read_b128 v[6:9], v148 offset:24576
	v_and_b32_e32 v130, 0xffffffe0, v15
	s_mov_b32 s58, s56
	s_mov_b32 s59, s56
	s_mov_b32 s60, s56
	s_mov_b32 s61, s56
	s_mov_b32 s62, s56
	s_waitcnt vmcnt(4) lgkmcnt(1)
	v_mfma_f32_32x32x16_bf16 v[18:33], v[2:5], v[74:77], v[18:33]
	v_or_b32_e32 v2, 64, v226
	v_bitop3_b32 v2, v2, v90, v10 bitop3:0xde
	v_add_u32_e32 v147, 0, v2
	s_mov_b32 s63, s56
	s_mov_b32 s64, s56
	s_mov_b32 s65, s56
	s_mov_b32 s66, s56
	s_waitcnt lgkmcnt(0)
	v_mfma_f32_32x32x16_bf16 v[34:49], v[6:9], v[74:77], v[34:49]
	ds_read_b128 v[2:5], v147 offset:16384
	ds_read_b128 v[6:9], v147 offset:24576
	s_mov_b32 s67, s56
	s_mov_b32 s68, s56
	s_mov_b32 s69, s56
	s_mov_b32 s70, s56
	s_mov_b32 s71, s56
	s_mov_b32 s35, 4
	s_waitcnt vmcnt(3) lgkmcnt(1)
	v_mfma_f32_32x32x16_bf16 v[18:33], v[2:5], v[70:73], v[18:33]
	v_and_b32_e32 v2, 0x3fffffc0, v119
	v_lshl_add_u32 v131, v2, 2, 0
	v_or_b32_e32 v2, 0x60, v226
	v_bitop3_b32 v2, v2, v90, v10 bitop3:0xde
	v_add_u32_e32 v146, 0, v2
	ds_read_b128 v[2:5], v146 offset:16384
	v_lshl_add_u32 v138, v137, 2, v131
	s_waitcnt lgkmcnt(1)
	v_mfma_f32_32x32x16_bf16 v[34:49], v[6:9], v[70:73], v[34:49]
	v_and_b32_e32 v6, 0xc0, v58
	v_and_or_b32 v12, v11, 24, v6
	ds_read_b128 v[6:9], v146 offset:24576
	v_mov_b32_e32 v140, 0
	s_waitcnt vmcnt(2) lgkmcnt(1)
	v_mfma_f32_32x32x16_bf16 v[18:33], v[2:5], v[82:85], v[18:33]
	v_or_b32_e32 v2, 0x80, v226
	v_bitop3_b32 v14, v2, v90, v10 bitop3:0xde
	v_add_co_u32_e32 v2, vcc, s1, v54
	s_movk_i32 s1, 0x6000
	s_nop 0
	v_addc_co_u32_e32 v3, vcc, 0, v55, vcc
	global_load_dwordx4 v[58:61], v[2:3], off
	v_add_co_u32_e32 v2, vcc, s6, v56
	v_add_u32_e32 v150, 0, v14
	s_nop 0
	v_addc_co_u32_e32 v3, vcc, 0, v57, vcc
	v_add_co_u32_e32 v4, vcc, s1, v56
	s_waitcnt lgkmcnt(0)
	v_mfma_f32_32x32x16_bf16 v[34:49], v[6:9], v[82:85], v[34:49]
	v_addc_co_u32_e32 v5, vcc, 0, v57, vcc
	global_load_dwordx4 v[62:65], v[2:3], off
	global_load_dwordx4 v[102:105], v[4:5], off
	ds_read_b128 v[2:5], v150 offset:16384
	v_and_b32_e32 v6, 32, v13
	v_and_b32_e32 v7, 0x100, v11
	v_or3_b32 v133, v12, v6, v7
	ds_read_b128 v[6:9], v150 offset:24576
	s_waitcnt vmcnt(4) lgkmcnt(1)
	v_mfma_f32_32x32x16_bf16 v[18:33], v[2:5], v[78:81], v[18:33]
	v_or_b32_e32 v2, 0xa0, v226
	v_bitop3_b32 v2, v2, v90, v10 bitop3:0xde
	v_add_u32_e32 v149, 0, v2
	ds_read_b128 v[2:5], v149 offset:16384
	ds_read_b128 v[90:93], v149 offset:24576
	s_cselect_b32 s1, 0, 0
	v_add_u32_e32 v141, s1, v133
	s_waitcnt lgkmcnt(2)
	v_mfma_f32_32x32x16_bf16 v[34:49], v[6:9], v[78:81], v[34:49]
	s_waitcnt vmcnt(3) lgkmcnt(1)
	v_mfma_f32_32x32x16_bf16 v[18:33], v[2:5], v[66:69], v[18:33]
	v_mov_b64_e32 v[2:3], s[56:57]
	v_mov_b64_e32 v[16:17], s[70:71]
	v_mov_b64_e32 v[4:5], s[58:59]
	v_mov_b64_e32 v[6:7], s[60:61]
	v_mov_b64_e32 v[8:9], s[62:63]
	v_mov_b64_e32 v[10:11], s[64:65]
	v_mov_b64_e32 v[12:13], s[66:67]
	s_waitcnt lgkmcnt(0)
	v_mfma_f32_32x32x16_bf16 v[34:49], v[90:93], v[66:69], v[34:49]
	s_nop 2
	v_max_f32_e32 v90, v19, v19
	v_max_f32_e32 v91, v18, v18
	v_max_f32_e32 v90, v91, v90
	v_max3_f32 v90, v90, v20, v21
	v_max3_f32 v90, v90, v22, v23
	v_max3_f32 v90, v90, v24, v25
	v_max3_f32 v90, v90, v26, v27
	v_max3_f32 v90, v90, v28, v29
	v_max3_f32 v90, v90, v30, v31
	v_max3_f32 v90, v90, v32, v33
	v_max3_f32 v90, v90, v34, v35
	v_max3_f32 v90, v90, v36, v37
	v_max3_f32 v90, v90, v38, v39
	v_max3_f32 v90, v90, v40, v41
	v_max3_f32 v90, v90, v42, v43
	v_max3_f32 v90, v90, v44, v45
	v_max3_f32 v90, v90, v46, v47
	v_max3_f32 v90, v90, v48, v49
	v_mov_b32_e32 v91, v90
	s_nop 1
	v_permlane32_swap_b32_e32 v90, v91
	v_max_f32_e32 v91, v91, v91
	v_max_f32_e32 v90, v90, v90
	v_max_f32_e32 v106, v90, v91
	v_add_f32_e32 v90, 0x7149f2ca, v106
	v_cmp_ge_f32_e32 vcc, s93, v90
	v_add_co_u32_e64 v90, s[4:5], s4, v56
	s_cmp_eq_u64 vcc, exec
	s_nop 0
	v_addc_co_u32_e64 v91, s[4:5], 0, v57, s[4:5]
	v_add_co_u32_e64 v56, s[4:5], s49, v56
	s_cselect_b64 vcc, -1, 0
	s_nop 0
	v_addc_co_u32_e64 v57, s[4:5], 0, v57, s[4:5]
	v_add_co_u32_e64 v54, s[4:5], s6, v54
	global_load_dwordx4 v[94:97], v[90:91], off
	global_load_dwordx4 v[98:101], v[56:57], off
	v_addc_co_u32_e64 v55, s[4:5], 0, v55, s[4:5]
	global_load_dwordx4 v[90:93], v[54:55], off
	v_max_f32_e32 v55, 0xf149f2ca, v106
	v_mov_b32_e32 v54, 0xf149f2ca
	v_cndmask_b32_e32 v118, v55, v54, vcc
	v_mul_f32_e32 v54, 0xbfb8aa3b, v118
	v_fmamk_f32 v18, v18, 0x3fb8aa3b, v54
	v_exp_f32_e32 v128, v18
	v_fmamk_f32 v18, v19, 0x3fb8aa3b, v54
	v_exp_f32_e32 v157, v18
	v_fmamk_f32 v18, v20, 0x3fb8aa3b, v54
	v_exp_f32_e32 v129, v18
	v_fmamk_f32 v18, v21, 0x3fb8aa3b, v54
	v_exp_f32_e32 v158, v18
	v_fmamk_f32 v18, v22, 0x3fb8aa3b, v54
	v_exp_f32_e32 v155, v18
	v_fmamk_f32 v18, v23, 0x3fb8aa3b, v54
	v_exp_f32_e32 v159, v18
	v_fmamk_f32 v18, v24, 0x3fb8aa3b, v54
	v_exp_f32_e32 v156, v18
	v_fmamk_f32 v18, v25, 0x3fb8aa3b, v54
	v_exp_f32_e32 v160, v18
	v_fmamk_f32 v18, v26, 0x3fb8aa3b, v54
	v_exp_f32_e32 v120, v18
	v_fmamk_f32 v18, v27, 0x3fb8aa3b, v54
	v_exp_f32_e32 v124, v18
	v_fmamk_f32 v18, v28, 0x3fb8aa3b, v54
	v_exp_f32_e32 v121, v18
	v_fmamk_f32 v18, v29, 0x3fb8aa3b, v54
	v_exp_f32_e32 v125, v18
	v_fmamk_f32 v18, v30, 0x3fb8aa3b, v54
	s_addk_i32 s1, 0x2000
	s_mul_i32 s6, s0, 0x440000
	v_exp_f32_e32 v122, v18
	v_fmamk_f32 v18, v31, 0x3fb8aa3b, v54
	v_add_u32_e32 v139, s1, v133
	s_mul_hi_i32 s1, s0, 0x440000
	s_add_u32 s6, s6, s24
	v_exp_f32_e32 v126, v18
	v_fmamk_f32 v18, v32, 0x3fb8aa3b, v54
	s_addc_u32 s7, s1, s7
	v_pk_fma_f32 v[106:107], v[40:41], s[92:93], v[54:55] op_sel_hi:[1,0,0]
	v_sub_f32_e32 v40, 0xf149f2ca, v55
	v_exp_f32_e32 v123, v18
	v_lshl_add_u64 v[18:19], s[6:7], 0, v[52:53]
	s_mul_hi_i32 s1, s0, 0x220000
	s_mul_i32 s0, s0, 0x220000
	s_mul_i32 s7, s31, 0x88000
	v_mul_f32_e32 v40, 0x3fb8aa3b, v40
	v_and_b32_e32 v20, 15, v119
	s_mul_hi_i32 s6, s31, 0x88000
	s_add_u32 s0, s0, s7
	s_waitcnt vmcnt(3)
	s_waitcnt vmcnt(5)
	ds_write_b128 v144, v[58:61] offset:8192
	s_waitcnt vmcnt(4)
	ds_write_b128 v142, v[62:65] offset:32768
	s_waitcnt vmcnt(3)
	ds_write_b128 v143, v[102:105] offset:32768
	v_pk_fma_f32 v[102:103], v[48:49], s[92:93], v[54:55] op_sel_hi:[1,0,0]
	v_pk_fma_f32 v[108:109], v[46:47], s[92:93], v[54:55] op_sel_hi:[1,0,0]
	v_pk_fma_f32 v[110:111], v[44:45], s[92:93], v[54:55] op_sel_hi:[1,0,0]
	v_pk_fma_f32 v[104:105], v[42:43], s[92:93], v[54:55] op_sel_hi:[1,0,0]
	v_exp_f32_e32 v40, v40
	v_pk_fma_f32 v[112:113], v[38:39], s[92:93], v[54:55] op_sel_hi:[1,0,0]
	v_pk_fma_f32 v[114:115], v[36:37], s[92:93], v[54:55] op_sel_hi:[1,0,0]
	v_pk_fma_f32 v[116:117], v[34:35], s[92:93], v[54:55] op_sel_hi:[1,0,0]
	v_fmac_f32_e32 v54, 0x3fb8aa3b, v33
	v_lshl_or_b32 v18, v20, 4, v18
	s_addc_u32 s1, s1, s6
	v_exp_f32_e32 v127, v54
	v_cmp_gt_u32_e64 s[4:5], 32, v132
	v_lshl_add_u64 v[132:133], s[18:19], 0, v[18:19]
	v_lshl_add_u64 v[18:19], s[0:1], 0, v[50:51]
	v_and_b32_e32 v20, 7, v119
	v_lshl_or_b32 v18, v20, 4, v18
	v_mov_b64_e32 v[14:15], s[68:69]
	v_lshl_add_u64 v[134:135], s[20:21], 0, v[18:19]
	v_mov_b64_e32 v[32:33], v[16:17]
	v_readlane_b32 s60, v255, 19
	v_readlane_b32 s62, v255, 21
	v_readlane_b32 s64, v255, 23
	v_readlane_b32 s66, v255, 25
	v_cndmask_b32_e64 v151, v40, 1.0, vcc
	v_mov_b64_e32 v[30:31], v[14:15]
	v_mov_b64_e32 v[28:29], v[12:13]
	v_mov_b64_e32 v[26:27], v[10:11]
	v_mov_b64_e32 v[24:25], v[8:9]
	v_mov_b64_e32 v[22:23], v[6:7]
	v_mov_b64_e32 v[20:21], v[4:5]
	v_mov_b64_e32 v[18:19], v[2:3]
	v_readlane_b32 s61, v255, 20
	v_readlane_b32 s63, v255, 22
	v_readlane_b32 s65, v255, 24
	v_readlane_b32 s67, v255, 26
	s_waitcnt lgkmcnt(0)
	s_barrier

.LBB0_600:
	s_setprio 0
	s_mov_b64 s[58:59], s[72:73]
	v_mov_b32_e32 v2, v0
	s_mov_b32 s57, s2
	v_writelane_b32 v255, s38, 29
	s_barrier
	s_cmpk_gt_i32 s57, 0xff
	v_readfirstlane_b32 s0, v2
	v_writelane_b32 v255, s39, 30
	s_cbranch_scc1 .LBB0_844
	s_ashr_i32 s95, s0, 6
	s_cmp_lt_i32 s95, 4
	s_cselect_b64 s[64:65], -1, 0
	s_add_i32 s6, s95, -4
	s_cmp_eq_u32 s6, 2
	s_movk_i32 s0, 0x6000
	s_cselect_b32 s0, s0, 0x8000
	s_cmp_lg_u32 s6, 1
	s_cselect_b32 s7, s0, 0x2000
	s_cmp_lg_u32 s6, 0
	s_cselect_b64 s[0:1], -1, 0
	v_writelane_b32 v255, s0, 31
	v_and_b32_e32 v5, 7, v2
	v_bfe_u32 v98, v2, 3, 3
	v_writelane_b32 v255, s1, 32
	s_and_b64 s[0:1], s[0:1], exec
	v_lshlrev_b32_e32 v84, 3, v5
	s_cselect_b32 s0, s7, 0
	v_lshlrev_b32_e32 v8, 8, v98
	v_lshlrev_b32_e32 v5, 5, v5
	v_or3_b32 v99, s0, v8, v5
	s_lshl_b32 s0, s6, 3
	v_or_b32_e32 v100, s0, v98
	v_cmp_lt_i32_e64 s[8:9], s87, v100
	s_cmp_eq_u32 s6, 3
	v_and_b32_e32 v3, 63, v2
	v_writelane_b32 v255, s8, 33
	v_and_b32_e32 v85, 15, v2
	v_bfe_u32 v4, v2, 4, 2
	v_writelane_b32 v255, s9, 34
	s_cselect_b64 s[8:9], -1, 0
	s_cmp_lg_u32 s6, 3
	s_cselect_b64 s[66:67], -1, 0
	s_add_i32 s0, s0, 32
	v_writelane_b32 v255, s8, 35
	v_or_b32_e32 v105, s0, v98
	v_cmp_lt_i32_e64 s[0:1], s87, v105
	v_writelane_b32 v255, s9, 36
	v_lshlrev_b32_e32 v6, 3, v2
	v_writelane_b32 v255, s0, 37
	v_bfe_u32 v7, v2, 2, 1
	v_bfe_u32 v103, v2, 1, 5
	v_writelane_b32 v255, s1, 38
	s_lshl_b32 s0, s79, 2
	v_lshrrev_b32_e32 v2, 1, v2
	s_abs_i32 s7, s0
	v_and_b32_e32 v114, 28, v2
	v_cvt_f32_u32_e32 v2, s7
	v_readlane_b32 s8, v255, 12
	v_readlane_b32 s9, v255, 13
	s_lshl_b64 s[68:69], s[8:9], 26
	v_rcp_iflag_f32_e32 v2, v2
	s_sub_i32 s8, 0, s7
	s_add_i32 s1, s0, 0x5fff
	s_xor_b32 s0, s1, s0
	v_mul_f32_e32 v2, 0x4f7ffffe, v2
	v_cvt_u32_f32_e32 v2, v2
	s_abs_i32 s1, s1
	s_ashr_i32 s0, s0, 31
	v_lshl_or_b32 v82, s95, 2, v4
	v_readfirstlane_b32 s9, v2
	s_mul_i32 s8, s8, s9
	s_mul_hi_u32 s8, s9, s8
	s_add_i32 s9, s9, s8
	s_mul_hi_u32 s8, s1, s9
	s_mul_i32 s9, s8, s7
	s_sub_i32 s1, s1, s9
	s_add_i32 s9, s8, 1
	s_sub_i32 s33, s1, s7
	s_cmp_ge_u32 s1, s7
	s_cselect_b32 s8, s9, s8
	s_cselect_b32 s1, s33, s1
	s_add_i32 s9, s8, 1
	s_cmp_ge_u32 s1, s7
	s_cselect_b32 s1, s9, s8
	s_xor_b32 s1, s1, s0
	v_and_b32_e32 v4, 8, v6
	v_lshlrev_b32_e32 v101, 5, v3
	v_lshlrev_b32_e32 v109, 4, v7
	v_lshl_or_b32 v111, v100, 8, v5
	s_sub_i32 s0, s1, s0
	v_lshl_or_b32 v121, s95, 3, v98
	v_ashrrev_i32_e32 v83, 31, v82
	v_lshlrev_b32_e32 v87, 4, v85
	v_lshlrev_b32_e32 v96, 2, v82
	v_cmp_eq_u32_e64 s[4:5], 15, v85
	v_or_b32_e32 v97, 16, v85
	v_add_u32_e32 v102, 0xffffff00, v100
	v_or_b32_e32 v104, 0x8000, v103
	v_add_u32_e32 v106, 0xffffff00, v105
	v_or_b32_e32 v107, 0x8020, v103
	v_cmp_eq_u32_e64 s[10:11], 0, v7
	v_add_u32_e32 v108, 0, v99
	v_xor_b32_e32 v110, 16, v109
	v_add_u32_e32 v112, 0, v111
	v_add_u32_e32 v113, 0, v101
	v_and_b32_e32 v86, 56, v6
	v_cmp_eq_u32_e64 s[12:13], 14, v85
	v_cmp_eq_u32_e64 s[14:15], 0, v85
	v_cmp_eq_u32_e64 s[16:17], 1, v85
	v_cmp_eq_u32_e64 s[18:19], 2, v85
	v_cmp_eq_u32_e64 s[20:21], 3, v85
	v_cmp_eq_u32_e64 s[22:23], 4, v85
	v_cmp_eq_u32_e64 s[24:25], 5, v85
	v_cmp_eq_u32_e64 s[26:27], 6, v85
	v_cmp_eq_u32_e64 s[28:29], 7, v85
	v_cmp_eq_u32_e64 s[30:31], 8, v85
	v_cmp_eq_u32_e64 s[34:35], 9, v85
	v_cmp_eq_u32_e64 s[36:37], 10, v85
	v_cmp_eq_u32_e64 s[38:39], 11, v85
	v_cmp_eq_u32_e64 s[40:41], 12, v85
	v_cmp_eq_u32_e64 s[42:43], 13, v85
	v_or_b32_e32 v115, 8, v98
	v_or_b32_e32 v116, 16, v98
	v_or_b32_e32 v117, 24, v98
	v_or_b32_e32 v118, 0x68, v98
	v_or_b32_e32 v119, 0x70, v98
	v_or_b32_e32 v120, 0x78, v98
	v_writelane_b32 v255, s0, 39
	v_sub_u32_e32 v122, 0x10bf, v121
	s_mul_i32 s80, s79, s6
	v_lshlrev_b32_e32 v88, 1, v4
	s_branch .LBB0_604
